# speedup vs baseline: 1.0884x; 1.0005x over previous
.LBB2_97:
	ds_read_b128 v[2:5], v125 offset:40960
	ds_read_b128 v[48:51], v125 offset:41984
	v_cvt_pkrtz_f16_f32 v44, v95, v94
	v_cvt_pkrtz_f16_f32 v45, v97, v96
	v_cvt_pkrtz_f16_f32 v46, v99, v98
	v_cvt_pkrtz_f16_f32 v47, v35, v34
	v_cvt_pkrtz_f16_f32 v34, v37, v36
	v_cvt_pkrtz_f16_f32 v35, v39, v38
	v_cvt_pkrtz_f16_f32 v36, v41, v40
	s_waitcnt lgkmcnt(1)
	v_mfma_f32_32x32x16_f16 v[2:17], v[2:5], v[44:47], 0
	v_cvt_pkrtz_f16_f32 v37, v19, v18
	ds_read_b128 v[38:41], v125 offset:43008
	v_add_u32_e32 v92, 0, v90
	s_mov_b32 s4, 0xff61b1e6
	v_mov_b32_e32 v91, 0
	s_waitcnt lgkmcnt(1)
	v_mfma_f32_32x32x16_f16 v[2:17], v[48:51], v[34:37], v[2:17]
	v_cvt_pkrtz_f16_f32 v48, v21, v20
	v_cvt_pkrtz_f16_f32 v49, v23, v22
	v_cvt_pkrtz_f16_f32 v50, v42, v24
	v_cvt_pkrtz_f16_f32 v51, v43, v27
	ds_read_b128 v[18:21], v125 offset:44032
	s_waitcnt lgkmcnt(1)
	v_mfma_f32_32x32x16_f16 v[2:17], v[38:41], v[48:51], v[2:17]
	v_cvt_pkrtz_f16_f32 v38, v26, v25
	v_cvt_pkrtz_f16_f32 v39, v29, v28
	v_cvt_pkrtz_f16_f32 v40, v32, v30
	v_cvt_pkrtz_f16_f32 v41, v33, v31
	s_waitcnt lgkmcnt(0)
	s_nop 0
	v_mfma_f32_32x32x16_f16 v[2:17], v[18:21], v[38:41], v[2:17]
	ds_read_b128 v[18:21], v125 offset:45056
	ds_read_b128 v[52:55], v125 offset:46080
	ds_read_b128 v[94:97], v92 offset:62464
	ds_read_b128 v[98:101], v125 offset:47104
	ds_read_b128 v[102:105], v125 offset:48128
	s_waitcnt lgkmcnt(2)
	s_nop 5
	v_add_f32_e32 v56, v4, v96
	v_mfma_f32_32x32x16_f16 v[18:33], v[18:21], v[44:47], 0
	ds_read_b128 v[42:45], v92 offset:62496
	ds_read_b128 v[106:109], v92 offset:62528
	v_add_f32_e32 v46, v2, v94
	v_add_f32_e32 v47, v3, v95
	v_add_f32_e32 v57, v5, v97
	ds_read_b128 v[2:5], v92 offset:62560
	s_waitcnt lgkmcnt(2)
	v_add_f32_e32 v42, v6, v42
	s_waitcnt lgkmcnt(1)
	v_add_f32_e32 v10, v10, v106
	v_mfma_f32_32x32x16_f16 v[18:33], v[52:55], v[34:37], v[18:33]
	v_add_f32_e32 v34, v7, v43
	v_add_f32_e32 v35, v8, v44
	v_add_f32_e32 v36, v9, v45
	s_waitcnt lgkmcnt(0)
	v_add_f32_e32 v14, v14, v2
	v_add_f32_e32 v15, v15, v3
	v_add_f32_e32 v16, v16, v4
	v_add_f32_e32 v17, v17, v5
	v_mfma_f32_32x32x16_f16 v[18:33], v[98:101], v[48:51], v[18:33]
	ds_read_b128 v[2:5], v92 offset:62592
	ds_read_b128 v[6:9], v92 offset:62624
	v_max_f32_e32 v37, 0, v42
	v_max_f32_e32 v34, 0, v34
	v_max_f32_e32 v35, 0, v35
	v_max_f32_e32 v36, 0, v36
	v_add_f32_e32 v11, v11, v107
	v_add_f32_e32 v12, v12, v108
	v_mfma_f32_32x32x16_f16 v[18:33], v[102:105], v[38:41], v[18:33]
	v_add_f32_e32 v13, v13, v109
	v_max_f32_e32 v38, 0, v10
	v_max_f32_e32 v39, 0, v11
	v_max_f32_e32 v40, 0, v12
	v_max_f32_e32 v41, 0, v13
	v_max_f32_e32 v42, 0, v14
	v_max_f32_e32 v43, 0, v15
	s_waitcnt lgkmcnt(1)
	s_nop 3
	v_add_f32_e32 v18, v18, v2
	v_add_f32_e32 v19, v19, v3
	v_add_f32_e32 v20, v20, v4
	v_add_f32_e32 v21, v21, v5
	ds_read_b128 v[2:5], v92 offset:62656
	s_waitcnt lgkmcnt(1)
	v_add_f32_e32 v22, v22, v6
	v_add_f32_e32 v23, v23, v7
	v_add_f32_e32 v24, v24, v8
	v_add_f32_e32 v25, v25, v9
	ds_read_b128 v[6:9], v92 offset:62688
	s_waitcnt lgkmcnt(1)
	v_add_f32_e32 v26, v26, v2
	v_add_f32_e32 v27, v27, v3
	v_add_f32_e32 v28, v28, v4
	v_add_f32_e32 v29, v29, v5
	ds_read_b128 v[2:5], v125 offset:49152
	s_waitcnt lgkmcnt(1)
	v_add_f32_e32 v30, v30, v6
	v_add_f32_e32 v31, v31, v7
	v_add_f32_e32 v32, v32, v8
	v_add_f32_e32 v33, v33, v9
	v_max_f32_e32 v6, 0, v46
	v_max_f32_e32 v7, 0, v47
	v_max_f32_e32 v8, 0, v56
	v_max_f32_e32 v9, 0, v57
	v_max_f32_e32 v46, 0, v18
	v_max_f32_e32 v47, 0, v19
	v_max_f32_e32 v48, 0, v20
	v_max_f32_e32 v49, 0, v21
	v_cvt_pkrtz_f16_f32 v6, v6, v7
	v_cvt_pkrtz_f16_f32 v7, v8, v9
	v_cvt_pkrtz_f16_f32 v8, v37, v34
	v_cvt_pkrtz_f16_f32 v9, v35, v36
	ds_read_b128 v[18:21], v125 offset:50176
	v_max_f32_e32 v44, 0, v16
	v_max_f32_e32 v45, 0, v17
	s_waitcnt lgkmcnt(1)
	v_mfma_f32_32x32x16_f16 v[2:17], v[2:5], v[6:9], 0
	v_max_f32_e32 v50, 0, v22
	v_max_f32_e32 v51, 0, v23
	v_max_f32_e32 v52, 0, v24
	v_max_f32_e32 v53, 0, v25
	v_max_f32_e32 v54, 0, v26
	v_max_f32_e32 v55, 0, v27
	v_max_f32_e32 v34, 0, v28
	v_max_f32_e32 v35, 0, v29
	v_cvt_pkrtz_f16_f32 v22, v38, v39
	v_cvt_pkrtz_f16_f32 v23, v40, v41
	v_cvt_pkrtz_f16_f32 v24, v42, v43
	v_cvt_pkrtz_f16_f32 v25, v44, v45
	ds_read_b128 v[26:29], v125 offset:51200
	v_max_f32_e32 v30, 0, v30
	s_waitcnt lgkmcnt(1)
	v_mfma_f32_32x32x16_f16 v[2:17], v[18:21], v[22:25], v[2:17]
	v_cvt_pkrtz_f16_f32 v18, v46, v47
	v_cvt_pkrtz_f16_f32 v19, v48, v49
	v_cvt_pkrtz_f16_f32 v20, v50, v51
	v_cvt_pkrtz_f16_f32 v21, v52, v53
	ds_read_b128 v[22:25], v125 offset:52224
	v_max_f32_e32 v31, 0, v31
	s_waitcnt lgkmcnt(1)
	v_mfma_f32_32x32x16_f16 v[2:17], v[26:29], v[18:21], v[2:17]
	v_max_f32_e32 v21, 0, v32
	v_max_f32_e32 v26, 0, v33
	v_cvt_pkrtz_f16_f32 v18, v54, v55
	v_cvt_pkrtz_f16_f32 v19, v34, v35
	v_cvt_pkrtz_f16_f32 v20, v30, v31
	v_cvt_pkrtz_f16_f32 v21, v21, v26
	ds_read_b128 v[26:29], v92 offset:62720
	s_waitcnt lgkmcnt(1)
	v_mfma_f32_32x32x16_f16 v[2:17], v[22:25], v[18:21], v[2:17]
	s_nop 11
	ds_read_b128 v[10:13], v92 offset:62752
	s_waitcnt lgkmcnt(1)
	v_add_f32_e32 v2, v26, v2
	v_add_f32_e32 v3, v27, v3
	v_max3_f32 v15, v2, s4, v3
	v_add_f32_e32 v16, v28, v4
	v_add_f32_e32 v17, v29, v5
	v_max3_f32 v4, v15, v16, v17
	s_waitcnt lgkmcnt(0)
	v_add_f32_e32 v15, v10, v6
	v_add_f32_e32 v18, v11, v7
	v_max3_f32 v4, v4, v15, v18
	v_add_f32_e32 v12, v12, v8
	v_add_f32_e32 v13, v13, v9
	v_max3_f32 v4, v4, v12, v13
	v_mov_b32_e32 v5, v4
	v_mov_b32_e32 v6, v4
	s_nop 1
	v_permlane32_swap_b32_e32 v5, v6
	v_cndmask_b32_e64 v5, v5, v6, s[2:3]
	v_max_f32_e32 v5, v5, v5
	v_max_f32_e32 v19, v4, v5
	v_sub_f32_e32 v2, v2, v19
	v_mul_f32_e32 v2, 0x3fb8aa3b, v2
	v_exp_f32_e32 v10, v2
	v_sub_f32_e32 v2, v3, v19
	v_lshl_add_u32 v14, s28, 6, v92
	v_mul_f32_e32 v2, 0x3fb8aa3b, v2
	v_exp_f32_e32 v11, v2
	ds_read_b128 v[2:5], v14 offset:63808
	v_add_f32_e32 v6, 0, v10
	v_add_f32_e32 v20, v6, v11
	ds_read_b128 v[6:9], v14 offset:63840
	s_waitcnt lgkmcnt(1)
	v_pk_mul_f32 v[2:3], v[10:11], v[2:3]
	v_sub_f32_e32 v10, v16, v19
	v_mul_f32_e32 v10, 0x3fb8aa3b, v10
	v_sub_f32_e32 v11, v17, v19
	v_exp_f32_e32 v10, v10
	v_mul_f32_e32 v11, 0x3fb8aa3b, v11
	v_exp_f32_e32 v11, v11
	v_add_f32_e32 v2, 0, v2
	v_add_f32_e32 v14, v2, v3
	v_add_f32_e32 v2, v20, v10
	v_add_f32_e32 v16, v2, v11
	v_pk_mul_f32 v[2:3], v[10:11], v[4:5]
	v_sub_f32_e32 v4, v15, v19
	v_mul_f32_e32 v4, 0x3fb8aa3b, v4
	v_sub_f32_e32 v5, v18, v19
	v_exp_f32_e32 v4, v4
	v_mul_f32_e32 v5, 0x3fb8aa3b, v5
	v_exp_f32_e32 v5, v5
	v_add_f32_e32 v2, v14, v2
	v_add_f32_e32 v10, v2, v3
	v_add_f32_e32 v2, v16, v4
	v_add_f32_e32 v11, v2, v5
	s_waitcnt lgkmcnt(0)
	v_pk_mul_f32 v[2:3], v[4:5], v[6:7]
	v_sub_f32_e32 v4, v12, v19
	v_mul_f32_e32 v4, 0x3fb8aa3b, v4
	v_sub_f32_e32 v5, v13, v19
	v_exp_f32_e32 v4, v4
	v_mul_f32_e32 v5, 0x3fb8aa3b, v5
	v_exp_f32_e32 v5, v5
	v_add_f32_e32 v2, v10, v2
	v_add_f32_e32 v6, v2, v3
	v_add_f32_e32 v2, v11, v4
	v_add_f32_e32 v7, v2, v5
	v_pk_mul_f32 v[2:3], v[4:5], v[8:9]
	v_mov_b32_e32 v4, v7
	v_add_f32_e32 v2, v6, v2
	v_add_f32_e32 v2, v2, v3
	v_mov_b32_e32 v3, v7
	s_nop 1
	v_permlane32_swap_b32_e32 v3, v4
	v_cndmask_b32_e64 v3, v3, v4, s[2:3]
	v_add_f32_e32 v3, v7, v3
	v_mov_b32_e32 v4, v2
	v_mov_b32_e32 v5, v2
	v_rcp_f32_e32 v3, v3
	s_nop 0
	v_permlane32_swap_b32_e32 v4, v5
	v_cndmask_b32_e64 v4, v4, v5, s[2:3]
	v_add_f32_e32 v2, v2, v4
	v_mul_f32_e32 v14, v2, v3
	ds_read_b128 v[2:5], v125 offset:53248
	ds_read_b128 v[10:13], v125 offset:54272
	v_pk_add_f32 v[42:43], v[78:79], v[14:15] op_sel_hi:[1,0] neg_lo:[0,1] neg_hi:[0,1]
	v_pk_add_f32 v[44:45], v[80:81], v[14:15] op_sel_hi:[1,0] neg_lo:[0,1] neg_hi:[0,1]
	v_pk_add_f32 v[38:39], v[82:83], v[14:15] op_sel_hi:[1,0] neg_lo:[0,1] neg_hi:[0,1]
	v_pk_add_f32 v[40:41], v[84:85], v[14:15] op_sel_hi:[1,0] neg_lo:[0,1] neg_hi:[0,1]
	v_cvt_pkrtz_f16_f32 v6, v42, v43
	v_cvt_pkrtz_f16_f32 v7, v44, v45
	v_cvt_pkrtz_f16_f32 v8, v38, v39
	v_cvt_pkrtz_f16_f32 v9, v40, v41
	v_add_f32_e64 v34, v86, -v14
	v_add_f32_e64 v35, v87, -v14
	v_add_f32_e64 v36, v88, -v14
	v_add_f32_e64 v37, v89, -v14
	s_waitcnt lgkmcnt(1)
	v_mfma_f32_32x32x16_f16 v[18:33], v[2:5], v[6:9], 0
	v_add_f32_e64 v50, v72, -v14
	v_add_f32_e64 v51, v73, -v14
	v_add_f32_e64 v52, v74, -v14
	v_add_f32_e64 v53, v75, -v14
	v_add_f32_e64 v48, v68, -v14
	v_add_f32_e64 v49, v69, -v14
	v_pk_add_f32 v[54:55], v[70:71], v[14:15] op_sel_hi:[1,0] neg_lo:[0,1] neg_hi:[0,1]
	v_cvt_pkrtz_f16_f32 v68, v34, v35
	v_cvt_pkrtz_f16_f32 v69, v36, v37
	v_cvt_pkrtz_f16_f32 v70, v50, v51
	v_cvt_pkrtz_f16_f32 v71, v52, v53
	ds_read_b128 v[2:5], v125 offset:55296
	v_add_f32_e64 v46, v76, -v14
	v_add_f32_e64 v47, v77, -v14
	s_waitcnt lgkmcnt(1)
	v_mfma_f32_32x32x16_f16 v[18:33], v[10:13], v[68:71], v[18:33]
	v_add_f32_e64 v56, v58, -v14
	v_add_f32_e64 v57, v59, -v14
	v_cvt_pkrtz_f16_f32 v72, v46, v47
	v_cvt_pkrtz_f16_f32 v73, v48, v49
	v_cvt_pkrtz_f16_f32 v74, v54, v55
	v_cvt_pkrtz_f16_f32 v75, v56, v57
	ds_read_b128 v[10:13], v125 offset:56320
	v_add_f32_e64 v58, v66, -v14
	v_add_f32_e64 v59, v67, -v14
	s_waitcnt lgkmcnt(1)
	v_mfma_f32_32x32x16_f16 v[18:33], v[2:5], v[72:75], v[18:33]
	ds_read_b128 v[2:5], v125 offset:57344
	ds_read_b128 v[80:83], v125 offset:58368
	v_add_f32_e64 v60, v60, -v14
	v_add_f32_e64 v61, v61, -v14
	v_add_f32_e64 v62, v62, -v14
	v_add_f32_e64 v63, v63, -v14
	v_pk_add_f32 v[64:65], v[64:65], v[14:15] op_sel_hi:[1,0] neg_lo:[0,1] neg_hi:[0,1]
	v_cvt_pkrtz_f16_f32 v76, v58, v59
	v_cvt_pkrtz_f16_f32 v77, v60, v61
	v_cvt_pkrtz_f16_f32 v78, v62, v63
	v_cvt_pkrtz_f16_f32 v79, v64, v65
	s_waitcnt lgkmcnt(2)
	s_nop 0
	v_mfma_f32_32x32x16_f16 v[18:33], v[10:13], v[76:79], v[18:33]
	s_waitcnt lgkmcnt(1)
	v_mfma_f32_32x32x16_f16 v[2:17], v[2:5], v[6:9], 0
	s_waitcnt lgkmcnt(0)
	v_mfma_f32_32x32x16_f16 v[2:17], v[80:83], v[68:71], v[2:17]
	ds_read_b128 v[66:69], v125 offset:59392
	ds_read_b128 v[80:83], v125 offset:60416
	v_lshl_add_u64 v[70:71], v[118:119], 2, s[6:7]
	v_lshl_add_u64 v[70:71], v[70:71], 0, v[90:91]
	global_store_dwordx4 v[70:71], v[42:45], off
	global_store_dwordx4 v[70:71], v[38:41], off offset:32
	global_store_dwordx4 v[70:71], v[34:37], off offset:64
	global_store_dwordx4 v[70:71], v[50:53], off offset:96
	global_store_dwordx4 v[70:71], v[46:49], off offset:128
	global_store_dwordx4 v[70:71], v[54:57], off offset:160
	global_store_dwordx4 v[70:71], v[58:61], off offset:192
	global_store_dwordx4 v[70:71], v[62:65], off offset:224
	s_waitcnt lgkmcnt(1)
	v_mfma_f32_32x32x16_f16 v[2:17], v[66:69], v[72:75], v[2:17]
	s_waitcnt lgkmcnt(0)
	v_mfma_f32_32x32x16_f16 v[2:17], v[80:83], v[76:79], v[2:17]
	ds_read_b128 v[66:69], v92 offset:62784
	ds_read_b128 v[70:73], v92 offset:63040
	ds_read_b128 v[74:77], v92 offset:63296
	ds_read_b128 v[78:81], v92 offset:63552
	ds_read_b128 v[82:85], v92 offset:62816
	s_waitcnt lgkmcnt(4)
	v_add_f32_e32 v18, v66, v18
	v_mul_f32_e32 v18, 0x3f7fffac, v18
	v_add_f32_e32 v19, v67, v19
	s_waitcnt lgkmcnt(2)
	v_fma_f32 v18, v70, v18, v74
	v_mul_f32_e32 v19, 0x3f7fffac, v19
	v_max_f32_e32 v18, 0, v18
	v_fma_f32 v19, v71, v19, v75
	s_waitcnt lgkmcnt(1)
	v_fma_f32 v18, v78, v18, 0
	v_max_f32_e32 v19, 0, v19
	v_fmac_f32_e32 v18, v79, v19
	v_add_f32_e32 v19, v68, v20
	v_mul_f32_e32 v19, 0x3f7fffac, v19
	v_fma_f32 v19, v72, v19, v76
	v_max_f32_e32 v19, 0, v19
	v_fmac_f32_e32 v18, v80, v19
	v_add_f32_e32 v19, v69, v21
	ds_read_b128 v[86:89], v92 offset:63072
	ds_read_b128 v[94:97], v92 offset:63328
	v_mul_f32_e32 v19, 0x3f7fffac, v19
	v_fmac_f32_e32 v77, v73, v19
	ds_read_b128 v[98:101], v92 offset:63584
	v_max_f32_e32 v19, 0, v77
	v_fmac_f32_e32 v18, v81, v19
	s_waitcnt lgkmcnt(3)
	v_add_f32_e32 v19, v82, v22
	v_mul_f32_e32 v19, 0x3f7fffac, v19
	s_waitcnt lgkmcnt(1)
	v_fma_f32 v19, v86, v19, v94
	v_max_f32_e32 v19, 0, v19
	s_waitcnt lgkmcnt(0)
	v_fmac_f32_e32 v18, v98, v19
	v_add_f32_e32 v19, v83, v23
	v_mul_f32_e32 v19, 0x3f7fffac, v19
	v_fma_f32 v19, v87, v19, v95
	v_max_f32_e32 v19, 0, v19
	v_fmac_f32_e32 v18, v99, v19
	v_add_f32_e32 v19, v84, v24
	v_mul_f32_e32 v19, 0x3f7fffac, v19
	v_fma_f32 v19, v88, v19, v96
	v_max_f32_e32 v19, 0, v19
	v_fmac_f32_e32 v18, v100, v19
	v_add_f32_e32 v19, v85, v25
	v_mul_f32_e32 v19, 0x3f7fffac, v19
	v_fmac_f32_e32 v97, v89, v19
	v_max_f32_e32 v19, 0, v97
	ds_read_b128 v[20:23], v92 offset:62848
	ds_read_b128 v[66:69], v92 offset:63104
	ds_read_b128 v[70:73], v92 offset:63360
	ds_read_b128 v[74:77], v92 offset:63616
	ds_read_b128 v[78:81], v92 offset:62880
	v_fmac_f32_e32 v18, v101, v19
	s_waitcnt lgkmcnt(4)
	v_add_f32_e32 v19, v20, v26
	v_mul_f32_e32 v19, 0x3f7fffac, v19
	s_waitcnt lgkmcnt(2)
	v_fma_f32 v19, v66, v19, v70
	v_max_f32_e32 v19, 0, v19
	s_waitcnt lgkmcnt(1)
	v_fmac_f32_e32 v18, v74, v19
	v_add_f32_e32 v19, v21, v27
	v_mul_f32_e32 v19, 0x3f7fffac, v19
	v_fma_f32 v19, v67, v19, v71
	v_max_f32_e32 v19, 0, v19
	v_fmac_f32_e32 v18, v75, v19
	v_add_f32_e32 v19, v22, v28
	v_mul_f32_e32 v19, 0x3f7fffac, v19
	v_fma_f32 v19, v68, v19, v72
	v_max_f32_e32 v19, 0, v19
	v_fmac_f32_e32 v18, v76, v19
	v_add_f32_e32 v19, v23, v29
	ds_read_b128 v[82:85], v92 offset:63136
	ds_read_b128 v[86:89], v92 offset:63392
	v_mul_f32_e32 v19, 0x3f7fffac, v19
	v_fmac_f32_e32 v73, v69, v19
	ds_read_b128 v[94:97], v92 offset:63648
	v_max_f32_e32 v19, 0, v73
	v_fmac_f32_e32 v18, v77, v19
	s_waitcnt lgkmcnt(3)
	v_add_f32_e32 v19, v78, v30
	v_mul_f32_e32 v19, 0x3f7fffac, v19
	s_waitcnt lgkmcnt(1)
	v_fma_f32 v19, v82, v19, v86
	v_max_f32_e32 v19, 0, v19
	s_waitcnt lgkmcnt(0)
	v_fmac_f32_e32 v18, v94, v19
	v_add_f32_e32 v19, v79, v31
	v_mul_f32_e32 v19, 0x3f7fffac, v19
	v_fma_f32 v19, v83, v19, v87
	v_max_f32_e32 v19, 0, v19
	v_fmac_f32_e32 v18, v95, v19
	v_add_f32_e32 v19, v80, v32
	v_mul_f32_e32 v19, 0x3f7fffac, v19
	v_fma_f32 v19, v84, v19, v88
	v_max_f32_e32 v19, 0, v19
	v_fmac_f32_e32 v18, v96, v19
	v_add_f32_e32 v19, v81, v33
	ds_read_b128 v[20:23], v92 offset:62912
	ds_read_b128 v[24:27], v92 offset:63168
	ds_read_b128 v[28:31], v92 offset:63424
	ds_read_b128 v[66:69], v92 offset:63680
	ds_read_b128 v[70:73], v92 offset:62944
	v_mul_f32_e32 v19, 0x3f7fffac, v19
	s_waitcnt lgkmcnt(4)
	v_add_f32_e32 v2, v20, v2
	v_fmac_f32_e32 v89, v85, v19
	v_mul_f32_e32 v2, 0x3f7fffac, v2
	v_max_f32_e32 v19, 0, v89
	s_waitcnt lgkmcnt(2)
	v_fma_f32 v2, v24, v2, v28
	v_fmac_f32_e32 v18, v97, v19
	v_max_f32_e32 v2, 0, v2
	s_waitcnt lgkmcnt(1)
	v_fmac_f32_e32 v18, v66, v2
	v_add_f32_e32 v2, v21, v3
	v_mul_f32_e32 v2, 0x3f7fffac, v2
	v_fma_f32 v2, v25, v2, v29
	v_max_f32_e32 v2, 0, v2
	v_fmac_f32_e32 v18, v67, v2
	v_add_f32_e32 v2, v22, v4
	v_mul_f32_e32 v2, 0x3f7fffac, v2
	v_fma_f32 v2, v26, v2, v30
	v_max_f32_e32 v2, 0, v2
	v_fmac_f32_e32 v18, v68, v2
	v_add_f32_e32 v2, v23, v5
	ds_read_b128 v[74:77], v92 offset:63200
	ds_read_b128 v[78:81], v92 offset:63456
	v_mul_f32_e32 v2, 0x3f7fffac, v2
	v_fmac_f32_e32 v31, v27, v2
	ds_read_b128 v[82:85], v92 offset:63712
	v_max_f32_e32 v2, 0, v31
	v_fmac_f32_e32 v18, v69, v2
	s_waitcnt lgkmcnt(3)
	v_add_f32_e32 v2, v70, v6
	v_mul_f32_e32 v2, 0x3f7fffac, v2
	s_waitcnt lgkmcnt(1)
	v_fma_f32 v2, v74, v2, v78
	v_max_f32_e32 v2, 0, v2
	s_waitcnt lgkmcnt(0)
	v_fmac_f32_e32 v18, v82, v2
	v_add_f32_e32 v2, v71, v7
	v_mul_f32_e32 v2, 0x3f7fffac, v2
	v_fma_f32 v2, v75, v2, v79
	v_max_f32_e32 v2, 0, v2
	v_fmac_f32_e32 v18, v83, v2
	v_add_f32_e32 v2, v72, v8
	v_mul_f32_e32 v2, 0x3f7fffac, v2
	v_fma_f32 v2, v76, v2, v80
	v_max_f32_e32 v2, 0, v2
	v_fmac_f32_e32 v18, v84, v2
	v_add_f32_e32 v2, v73, v9
	v_mul_f32_e32 v2, 0x3f7fffac, v2
	v_fmac_f32_e32 v81, v77, v2
	v_max_f32_e32 v2, 0, v81
	v_fmac_f32_e32 v18, v85, v2
	ds_read_b128 v[2:5], v92 offset:62976
	ds_read_b128 v[6:9], v92 offset:63232
	ds_read_b128 v[20:23], v92 offset:63488
	ds_read_b128 v[24:27], v92 offset:63744
	ds_read_b128 v[28:31], v92 offset:63008
	s_waitcnt lgkmcnt(4)
	v_add_f32_e32 v2, v2, v10
	v_mul_f32_e32 v2, 0x3f7fffac, v2
	s_waitcnt lgkmcnt(2)
	v_fma_f32 v2, v6, v2, v20
	v_max_f32_e32 v2, 0, v2
	s_waitcnt lgkmcnt(1)
	v_fmac_f32_e32 v18, v24, v2
	v_add_f32_e32 v2, v3, v11
	v_mul_f32_e32 v2, 0x3f7fffac, v2
	v_fma_f32 v2, v7, v2, v21
	v_max_f32_e32 v2, 0, v2
	v_fmac_f32_e32 v18, v25, v2
	v_add_f32_e32 v2, v4, v12
	v_mul_f32_e32 v2, 0x3f7fffac, v2
	v_fma_f32 v2, v8, v2, v22
	v_max_f32_e32 v2, 0, v2
	v_fmac_f32_e32 v18, v26, v2
	v_add_f32_e32 v2, v5, v13
	ds_read_b128 v[66:69], v92 offset:63264
	ds_read_b128 v[70:73], v92 offset:63520
	v_mul_f32_e32 v2, 0x3f7fffac, v2
	v_fmac_f32_e32 v23, v9, v2
	ds_read_b128 v[74:77], v92 offset:63776
	v_max_f32_e32 v2, 0, v23
	v_fmac_f32_e32 v18, v27, v2
	s_waitcnt lgkmcnt(3)
	v_add_f32_e32 v2, v28, v14
	v_mul_f32_e32 v2, 0x3f7fffac, v2
	s_waitcnt lgkmcnt(1)
	v_fma_f32 v2, v66, v2, v70
	v_max_f32_e32 v2, 0, v2
	s_waitcnt lgkmcnt(0)
	v_fmac_f32_e32 v18, v74, v2
	v_add_f32_e32 v2, v29, v15
	v_mul_f32_e32 v2, 0x3f7fffac, v2
	v_fma_f32 v2, v67, v2, v71
	v_max_f32_e32 v2, 0, v2
	v_fmac_f32_e32 v18, v75, v2
	v_add_f32_e32 v2, v30, v16
	v_mul_f32_e32 v2, 0x3f7fffac, v2
	v_fma_f32 v2, v68, v2, v72
	v_max_f32_e32 v2, 0, v2
	v_fmac_f32_e32 v18, v76, v2
	v_add_f32_e32 v2, v31, v17
	v_mul_f32_e32 v2, 0x3f7fffac, v2
	v_fmac_f32_e32 v73, v69, v2
	v_max_f32_e32 v2, 0, v73
	v_fmac_f32_e32 v18, v77, v2
	v_mov_b32_e32 v2, v18
	v_mov_b32_e32 v3, v18
	s_nop 1
	v_permlane32_swap_b32_e32 v2, v3
	s_and_saveexec_b64 s[4:5], s[0:1]
	s_cbranch_execz .LBB2_99
	v_lshl_or_b32 v4, s12, 7, v1
	v_ashrrev_i32_e32 v5, 31, v4
	v_cndmask_b32_e64 v1, v2, v3, s[2:3]
	v_lshl_add_u64 v[4:5], v[4:5], 2, s[8:9]
	v_add_f32_e32 v1, v18, v1
	global_store_dword v[4:5], v1, off
